# static priority raise for waves 4-7 also in the attention phase (plus the RG-LRU phase)
# speedup vs baseline: 1.0099x; 1.0033x over previous
.LBB0_356:
	s_load_dwordx4 s[0:3], s[8:9], 0x138
	s_waitcnt lgkmcnt(0)
	s_mov_b64 s[4:5], s[0:1]
	s_cmp_lt_i32 s4, 4
	s_cselect_b64 s[0:1], -1, 0
	s_cmp_gt_i32 s5, 3
	s_cselect_b64 s[2:3], -1, 0
	s_and_b64 s[0:1], s[0:1], s[2:3]
	s_andn2_b64 vcc, exec, s[0:1]
	s_cbranch_vccnz .LBB0_462
	s_cmp_ge_u32 s33, 0x100
	s_cbranch_scc0 .Lp3_prio
	s_setprio 1
.Lp3_prio:
	s_mov_b64 s[10:11], s[8:9]
	s_waitcnt vmcnt(0)
	v_mbcnt_lo_u32_b32 v0, -1, 0
	v_mbcnt_hi_u32_b32 v0, -1, v0
	s_load_dwordx2 s[0:1], s[10:11], 0x130
	s_add_u32 s4, s8, 0x148
	s_addc_u32 s5, s9, 0
	v_readlane_b32 s2, v243, 0
	v_lshlrev_b32_e32 v87, 3, v0
	s_waitcnt lgkmcnt(0)
	s_add_u32 s6, s0, 0x13100000
	s_addc_u32 s7, s1, 0
	s_add_u32 s8, s0, 0x20900000
	s_addc_u32 s9, s1, 0
	s_cmpk_lt_i32 s2, 0x100
	v_readlane_b32 s3, v243, 1
	s_cbranch_scc1 .LBB0_359
	v_lshlrev_b32_e32 v78, 3, v0
	s_mov_b64 s[0:1], 0
	s_branch .LBB0_360

.LBB0_409:
	s_setprio 0
	v_readlane_b32 s6, v243, 7
	v_readlane_b32 s7, v243, 8
	s_load_dwordx4 s[0:3], s[6:7], 0x138
	s_waitcnt lgkmcnt(0)
	s_cmp_lt_i32 s1, 5
	s_mov_b64 s[0:1], -1
	s_cbranch_scc0 .LBB0_411
	s_waitcnt vmcnt(0)
	s_barrier
	s_mov_b64 s[0:1], 0
